# v6 plus a safety wait on the combine loop path without prefetch
# speedup vs baseline: 1.0039x; 1.0039x over previous
; #define CL_LOAD(r_) do { _Pragma("unroll") for (int j = 0; j < 4; ++j) xw[j] = *((const GAS v2u*)(XB + (size_t)(r_) * D) + lane + 64 * j); \
;         _Pragma("unroll") for (int k = 0; k < 4; ++k) { const GAS v2u* yr = (const GAS v2u*)(YE + ((size_t)(r_) * 4 + k) * D) + lane; _Pragma("unroll") for (int j = 0; j < 4; ++j) yw[k][j] = __builtin_nontemporal_load(yr + 64 * j); } } while (0)
; __device__ __forceinline__ void combine_ln_phase(Frame& F, const bf16* YE, const float* g, const float* b, float* X, bf16* XB) { LTID();
;     ...
;     if (gw < T) CL_LOAD(gw);
;     for (int row = gw; row < T; row += NGW) {
;         f32x4 v[4];
; #pragma unroll
;         for (int j = 0; j < 4; ++j) { const v2u w = xw[j]; v[j] = (f32x4){bflo(w.x), bfhi(w.x), bflo(w.y), bfhi(w.y)} * DN_ALPHA; }
; #pragma unroll
;         for (int k = 0; k < 4; ++k) {
; #pragma unroll
;             for (int j = 0; j < 4; ++j) { const v2u w = yw[k][j]; v[j].x += bflo(w.x); v[j].y += bfhi(w.x); v[j].z += bflo(w.y); v[j].w += bfhi(w.y); } }
;         if (row + NGW < T) CL_LOAD(row + NGW);
.LBB0_1235:
	s_add_i32 s6, s6, s2
	s_cmpk_gt_i32 s6, 0x7fff
	s_cselect_b64 s[10:11], -1, 0
	s_and_b64 vcc, exec, s[10:11]
	s_cbranch_vccnz .Lcomb_noload
	s_ashr_i32 s7, s6, 31
	s_lshl_b64 s[4:5], s[6:7], 11
	v_lshl_add_u64 v[28:29], v[22:23], 0, s[4:5]
	s_lshl_b64 s[4:5], s[6:7], 13
	s_add_u32 s4, s0, s4
	s_addc_u32 s5, s18, s5
	global_load_dwordx2 v[34:35], v[28:29], off
	global_load_dwordx2 v[32:33], v[28:29], off offset:512
	global_load_dwordx2 v[30:31], v[28:29], off offset:1024
	s_nop 0
	global_load_dwordx2 v[28:29], v[28:29], off offset:1536
	s_nop 0
	global_load_dwordx2 v[66:67], v0, s[4:5] nt
	global_load_dwordx2 v[64:65], v0, s[4:5] offset:512 nt
	global_load_dwordx2 v[62:63], v0, s[4:5] offset:1024 nt
	global_load_dwordx2 v[60:61], v0, s[4:5] offset:1536 nt
	global_load_dwordx2 v[58:59], v0, s[4:5] offset:2048 nt
	global_load_dwordx2 v[56:57], v0, s[4:5] offset:2560 nt
	global_load_dwordx2 v[54:55], v0, s[4:5] offset:3072 nt
	global_load_dwordx2 v[52:53], v0, s[4:5] offset:3584 nt
	v_lshl_add_u64 v[44:45], s[4:5], 0, v[0:1]
	s_mov_b64 s[4:5], 0x1000
	v_lshl_add_u64 v[36:37], v[44:45], 0, s[4:5]
	v_add_co_u32_e32 v46, vcc, 0x1000, v44
	s_mov_b64 s[4:5], 0x1800
	s_nop 0
	v_addc_co_u32_e32 v47, vcc, 0, v45, vcc
	v_lshl_add_u64 v[44:45], v[44:45], 0, s[4:5]
	global_load_dwordx2 v[42:43], v[46:47], off nt
	global_load_dwordx2 v[40:41], v[36:37], off offset:512 nt
	global_load_dwordx2 v[38:39], v[36:37], off offset:1024 nt
	s_nop 0
	global_load_dwordx2 v[36:37], v[36:37], off offset:1536 nt
	s_nop 0
	global_load_dwordx2 v[50:51], v[46:47], off offset:2048 nt
	global_load_dwordx2 v[48:49], v[44:45], off offset:512 nt
	s_nop 0
	global_load_dwordx2 v[46:47], v[44:45], off offset:1024 nt
	s_nop 0
	global_load_dwordx2 v[44:45], v[44:45], off offset:1536 nt
	s_branch .LBB0_1237
.Lcomb_noload:
	s_waitcnt vmcnt(0)
.LBB0_1237:
	v_lshlrev_b32_e32 v92, 16, v90
	v_and_b32_e32 v93, 0xffff0000, v90
	v_lshlrev_b32_e32 v90, 16, v91
	v_and_b32_e32 v91, 0xffff0000, v91
	v_lshlrev_b32_e32 v98, 16, v78
	v_and_b32_e32 v99, 0xffff0000, v78
	v_lshlrev_b32_e32 v100, 16, v79
	v_and_b32_e32 v101, 0xffff0000, v79
	v_lshlrev_b32_e32 v78, 16, v80
	v_and_b32_e32 v79, 0xffff0000, v80
	v_lshlrev_b32_e32 v80, 16, v81
	v_and_b32_e32 v81, 0xffff0000, v81
	v_pk_fma_f32 v[78:79], v[92:93], s[86:87], v[78:79] op_sel_hi:[1,0,1]
	v_lshlrev_b32_e32 v92, 16, v76
	v_and_b32_e32 v93, 0xffff0000, v76
	v_pk_fma_f32 v[80:81], v[90:91], s[86:87], v[80:81] op_sel_hi:[1,0,1]
	v_lshlrev_b32_e32 v76, 16, v77
	v_and_b32_e32 v77, 0xffff0000, v77
	v_pk_add_f32 v[76:77], v[80:81], v[76:77]
	v_lshlrev_b32_e32 v80, 16, v83
	v_and_b32_e32 v81, 0xffff0000, v83
	v_pk_add_f32 v[76:77], v[76:77], v[80:81]
	v_lshlrev_b32_e32 v80, 16, v89
	v_and_b32_e32 v81, 0xffff0000, v89
	v_lshlrev_b32_e32 v94, 16, v86
	v_and_b32_e32 v95, 0xffff0000, v86
	v_lshlrev_b32_e32 v86, 16, v87
	v_and_b32_e32 v87, 0xffff0000, v87
	v_pk_add_f32 v[80:81], v[76:77], v[80:81]
	v_lshlrev_b32_e32 v76, 16, v72
	v_and_b32_e32 v77, 0xffff0000, v72
	v_lshlrev_b32_e32 v72, 16, v73
	v_and_b32_e32 v73, 0xffff0000, v73
	v_pk_add_f32 v[78:79], v[78:79], v[92:93]
	v_lshlrev_b32_e32 v92, 16, v82
	v_and_b32_e32 v93, 0xffff0000, v82
	v_pk_fma_f32 v[76:77], v[94:95], s[86:87], v[76:77] op_sel_hi:[1,0,1]
	v_lshlrev_b32_e32 v82, 16, v68
	v_and_b32_e32 v83, 0xffff0000, v68
	v_pk_fma_f32 v[72:73], v[86:87], s[86:87], v[72:73] op_sel_hi:[1,0,1]
	v_lshlrev_b32_e32 v68, 16, v69
	v_and_b32_e32 v69, 0xffff0000, v69
	v_pk_add_f32 v[76:77], v[76:77], v[82:83]
	v_lshlrev_b32_e32 v82, 16, v70
	v_and_b32_e32 v83, 0xffff0000, v70
	v_pk_add_f32 v[68:69], v[72:73], v[68:69]
	v_lshlrev_b32_e32 v70, 16, v71
	v_and_b32_e32 v71, 0xffff0000, v71
	v_pk_add_f32 v[68:69], v[68:69], v[70:71]
	v_lshlrev_b32_e32 v70, 16, v75
	v_and_b32_e32 v71, 0xffff0000, v75
	v_lshlrev_b32_e32 v96, 16, v84
	v_and_b32_e32 v97, 0xffff0000, v84
	v_lshlrev_b32_e32 v84, 16, v85
	v_and_b32_e32 v85, 0xffff0000, v85
	v_pk_add_f32 v[72:73], v[68:69], v[70:71]
	v_lshlrev_b32_e32 v68, 16, v14
	v_and_b32_e32 v69, 0xffff0000, v14
	v_lshlrev_b32_e32 v14, 16, v15
	v_and_b32_e32 v15, 0xffff0000, v15
	v_pk_fma_f32 v[68:69], v[96:97], s[86:87], v[68:69] op_sel_hi:[1,0,1]
	v_lshlrev_b32_e32 v70, 16, v10
	v_and_b32_e32 v71, 0xffff0000, v10
	v_pk_fma_f32 v[14:15], v[84:85], s[86:87], v[14:15] op_sel_hi:[1,0,1]
	v_lshlrev_b32_e32 v10, 16, v11
	v_and_b32_e32 v11, 0xffff0000, v11
	v_pk_add_f32 v[68:69], v[68:69], v[70:71]
	v_lshlrev_b32_e32 v70, 16, v12
	v_and_b32_e32 v71, 0xffff0000, v12
	v_pk_add_f32 v[10:11], v[14:15], v[10:11]
	v_lshlrev_b32_e32 v12, 16, v13
	v_and_b32_e32 v13, 0xffff0000, v13
	v_pk_add_f32 v[10:11], v[10:11], v[12:13]
	v_lshlrev_b32_e32 v12, 16, v17
	v_and_b32_e32 v13, 0xffff0000, v17
	v_pk_add_f32 v[10:11], v[10:11], v[12:13]
	v_lshlrev_b32_e32 v12, 16, v6
	v_and_b32_e32 v13, 0xffff0000, v6
	v_lshlrev_b32_e32 v6, 16, v7
	v_and_b32_e32 v7, 0xffff0000, v7
	v_pk_fma_f32 v[12:13], v[98:99], s[86:87], v[12:13] op_sel_hi:[1,0,1]
	v_lshlrev_b32_e32 v14, 16, v2
	v_and_b32_e32 v15, 0xffff0000, v2
	v_pk_fma_f32 v[6:7], v[100:101], s[86:87], v[6:7] op_sel_hi:[1,0,1]
	v_lshlrev_b32_e32 v2, 16, v3
	v_and_b32_e32 v3, 0xffff0000, v3
	v_pk_add_f32 v[12:13], v[12:13], v[14:15]
	v_lshlrev_b32_e32 v14, 16, v4
	v_and_b32_e32 v15, 0xffff0000, v4
	v_pk_add_f32 v[2:3], v[6:7], v[2:3]
	v_lshlrev_b32_e32 v4, 16, v5
	v_and_b32_e32 v5, 0xffff0000, v5
	v_pk_add_f32 v[12:13], v[12:13], v[14:15]
	v_lshlrev_b32_e32 v14, 16, v8
	v_and_b32_e32 v15, 0xffff0000, v8
	v_pk_add_f32 v[2:3], v[2:3], v[4:5]
	v_lshlrev_b32_e32 v4, 16, v9
	v_and_b32_e32 v5, 0xffff0000, v9
	v_pk_add_f32 v[78:79], v[78:79], v[92:93]
; __device__ __forceinline__ float wave_sum(float v) { v = half_sum32(v); float a; const float b = swap32_other(v, a); return a + b; }
; #define GAS __attribute__((address_space(1)))
; __device__ __forceinline__ unsigned pk2(float lo, float hi) { f32x2_t v = {lo, hi}; bf16x2_t b = __builtin_convertvector(v, bf16x2_t); return __builtin_bit_cast(unsigned, b); }
; __device__ __forceinline__ void ln_apply(f32x4 (&v)[4], const float* g, const float* b, int lane) {
;     float s = 0.f;
; #pragma unroll
;     for (int j = 0; j < 4; ++j) s += (v[j].x + v[j].y) + (v[j].z + v[j].w);
;     const float mean = wave_sum(s) * (1.f / D); float s2 = 0.f;
; #pragma unroll
;     for (int j = 0; j < 4; ++j) { v[j] = v[j] - mean; s2 += (v[j].x * v[j].x + v[j].y * v[j].y) + (v[j].z * v[j].z + v[j].w * v[j].w); }
;     const float rstd = 1.f / sqrtf(wave_sum(s2) * (1.f / D) + LN_EPS);
; #pragma unroll
;     for (int j = 0; j < 4; ++j) { const f32x4 gg = *((const GAS f32x4*)g + lane + 64 * j), bb = *((const GAS f32x4*)b + lane + 64 * j); v[j] = v[j] * rstd * gg + bb; }
; }
; __device__ __forceinline__ void store_x(const f32x4 (&v)[4], float* X, bf16* XB, size_t row, int lane) {
;     GAS v2u* bo = (GAS v2u*)(XB + row * D) + lane;
; #pragma unroll
;     for (int j = 0; j < 4; ++j) { v2u w; w.x = pk2(v[j].x, v[j].y); w.y = pk2(v[j].z, v[j].w); bo[64 * j] = w; }
;     if (X) { GAS f32x4* xo = (GAS f32x4*)(X + row * D) + lane;
; #pragma unroll
;         for (int j = 0; j < 4; ++j) __builtin_nontemporal_store(v[j], xo + 64 * j); }
	v_lshlrev_b32_e32 v92, 16, v88
	v_and_b32_e32 v93, 0xffff0000, v88
	v_pk_add_f32 v[76:77], v[76:77], v[82:83]
	v_lshlrev_b32_e32 v82, 16, v74
	v_and_b32_e32 v83, 0xffff0000, v74
	v_pk_add_f32 v[68:69], v[68:69], v[70:71]
	v_lshlrev_b32_e32 v70, 16, v16
	v_and_b32_e32 v71, 0xffff0000, v16
	v_pk_add_f32 v[14:15], v[12:13], v[14:15]
	v_pk_add_f32 v[16:17], v[2:3], v[4:5]
	v_pk_add_f32 v[78:79], v[78:79], v[92:93]
	v_pk_add_f32 v[76:77], v[76:77], v[82:83]
	v_pk_add_f32 v[70:71], v[68:69], v[70:71]
	v_add_f32_e32 v2, v80, v81
	v_add_f32_e32 v3, v78, v79
	v_add_f32_e32 v2, v3, v2
	v_add_f32_e32 v3, v72, v73
	v_add_f32_e32 v4, v76, v77
	v_add_f32_e32 v2, 0, v2
	v_add_f32_e32 v3, v4, v3
	v_add_f32_e32 v2, v3, v2
	v_add_f32_e32 v3, v10, v11
	v_add_f32_e32 v4, v70, v71
	v_add_f32_e32 v3, v4, v3
	v_add_f32_e32 v2, v3, v2
	v_add_f32_e32 v3, v16, v17
	v_add_f32_e32 v4, v14, v15
	v_add_f32_e32 v3, v4, v3
	v_add_f32_e32 v2, v3, v2
	s_nop 1
	v_add_f32_dpp v2, v2, v2 quad_perm:[1,0,3,2] row_mask:0xf bank_mask:0xf bound_ctrl:1
	s_nop 1
	v_add_f32_dpp v2, v2, v2 quad_perm:[2,3,0,1] row_mask:0xf bank_mask:0xf bound_ctrl:1
	s_nop 1
	v_add_f32_dpp v2, v2, v2 row_half_mirror row_mask:0xf bank_mask:0xf bound_ctrl:1
	s_nop 1
	v_add_f32_dpp v2, v2, v2 row_mirror row_mask:0xf bank_mask:0xf bound_ctrl:1
	v_mov_b32_e32 v3, v2
	s_nop 1
	v_permlane16_swap_b32 v3, v2
	s_nop 0
	v_add_f32_e32 v2, v2, v3
	v_mov_b32_e32 v3, v2
	s_nop 1
	v_permlane32_swap_b32 v3, v2
	s_nop 0
	v_add_f32_e32 v2, v2, v3
	v_fmac_f32_e32 v81, 0xba800000, v2
	v_fmac_f32_e32 v79, 0xba800000, v2
	v_fmamk_f32 v80, v2, 0xba800000, v80
	v_fmamk_f32 v78, v2, 0xba800000, v78
	v_mul_f32_e32 v3, v79, v79
	v_mul_f32_e32 v4, v81, v81
	v_fmac_f32_e32 v3, v78, v78
	v_fmac_f32_e32 v4, v80, v80
	v_fmac_f32_e32 v73, 0xba800000, v2
	v_fmac_f32_e32 v77, 0xba800000, v2
	v_add_f32_e32 v3, v3, v4
	v_fmamk_f32 v72, v2, 0xba800000, v72
	v_fmamk_f32 v76, v2, 0xba800000, v76
	v_mul_f32_e32 v4, v77, v77
	v_mul_f32_e32 v5, v73, v73
	v_fmac_f32_e32 v4, v76, v76
	v_fmac_f32_e32 v5, v72, v72
	v_add_f32_e32 v4, v4, v5
	v_fmac_f32_e32 v11, 0xba800000, v2
	v_fmac_f32_e32 v71, 0xba800000, v2
	v_add_f32_e32 v3, v3, v4
	v_fmamk_f32 v10, v2, 0xba800000, v10
	v_fmamk_f32 v70, v2, 0xba800000, v70
	v_mul_f32_e32 v4, v71, v71
	v_mul_f32_e32 v5, v11, v11
	v_fmac_f32_e32 v4, v70, v70
	v_fmac_f32_e32 v5, v10, v10
	v_add_f32_e32 v4, v4, v5
	v_fmac_f32_e32 v17, 0xba800000, v2
	v_fmac_f32_e32 v15, 0xba800000, v2
	v_add_f32_e32 v3, v4, v3
	v_fmamk_f32 v16, v2, 0xba800000, v16
	v_fmamk_f32 v14, v2, 0xba800000, v14
	v_mul_f32_e32 v2, v15, v15
	v_mul_f32_e32 v4, v17, v17
	v_fmac_f32_e32 v2, v14, v14
	v_fmac_f32_e32 v4, v16, v16
	v_add_f32_e32 v2, v2, v4
	v_add_f32_e32 v2, v2, v3
	s_nop 1
	v_add_f32_dpp v2, v2, v2 quad_perm:[1,0,3,2] row_mask:0xf bank_mask:0xf bound_ctrl:1
	s_nop 1
	v_add_f32_dpp v2, v2, v2 quad_perm:[2,3,0,1] row_mask:0xf bank_mask:0xf bound_ctrl:1
	s_nop 1
	v_add_f32_dpp v2, v2, v2 row_half_mirror row_mask:0xf bank_mask:0xf bound_ctrl:1
	s_nop 1
	v_add_f32_dpp v2, v2, v2 row_mirror row_mask:0xf bank_mask:0xf bound_ctrl:1
	v_mov_b32_e32 v3, v2
	s_nop 1
	v_permlane16_swap_b32 v3, v2
	s_nop 0
	v_add_f32_e32 v2, v2, v3
	v_mov_b32_e32 v3, v2
	s_nop 1
	v_permlane32_swap_b32 v3, v2
	s_nop 0
	v_add_f32_e32 v2, v2, v3
	v_fmamk_f32 v2, v2, 0x3a800000, v228
	v_cmp_gt_f32_e32 vcc, s3, v2
	v_mul_f32_e32 v3, 0x4f800000, v2
	s_nop 0
	v_cndmask_b32_e32 v2, v2, v3, vcc
	v_sqrt_f32_e32 v3, v2
	s_nop 0
	v_add_u32_e32 v4, -1, v3
	v_fma_f32 v5, -v4, v3, v2
	v_cmp_ge_f32_e64 s[4:5], 0, v5
	v_add_u32_e32 v5, 1, v3
	s_nop 0
	v_cndmask_b32_e64 v4, v3, v4, s[4:5]
	v_fma_f32 v3, -v5, v3, v2
	v_cmp_lt_f32_e64 s[4:5], 0, v3
	s_nop 1
	v_cndmask_b32_e64 v3, v4, v5, s[4:5]
	v_mul_f32_e32 v4, 0x37800000, v3
	v_cndmask_b32_e32 v3, v3, v4, vcc
	v_cmp_class_f32_e32 vcc, v2, v229
	s_nop 1
	v_cndmask_b32_e32 v2, v3, v2, vcc
	v_div_scale_f32 v3, s[4:5], v2, v2, 1.0
	v_rcp_f32_e32 v4, v3
	s_nop 0
	v_fma_f32 v5, -v3, v4, 1.0
	v_fmac_f32_e32 v4, v5, v4
	v_div_scale_f32 v5, vcc, 1.0, v2, 1.0
	v_mul_f32_e32 v6, v5, v4
	v_fma_f32 v7, -v3, v6, v5
	v_fmac_f32_e32 v6, v7, v4
	v_fma_f32 v3, -v3, v6, v5
	v_div_fmas_f32 v3, v3, v4, v6
	v_div_fixup_f32 v68, v3, v2, 1.0
	v_pk_mul_f32 v[12:13], v[78:79], v[68:69] op_sel_hi:[1,0]
	v_pk_mul_f32 v[74:75], v[80:81], v[68:69] op_sel_hi:[1,0]
	v_pk_mul_f32 v[72:73], v[72:73], v[68:69] op_sel_hi:[1,0]
	v_pk_mul_f32 v[70:71], v[70:71], v[68:69] op_sel_hi:[1,0]
	v_pk_mul_f32 v[10:11], v[10:11], v[68:69] op_sel_hi:[1,0]
	v_pk_mul_f32 v[14:15], v[14:15], v[68:69] op_sel_hi:[1,0]
	v_pk_mul_f32 v[16:17], v[16:17], v[68:69] op_sel_hi:[1,0]
	s_andn2_b64 vcc, exec, s[8:9]
	s_waitcnt vmcnt(20)
	v_pk_fma_f32 v[4:5], v[112:113], v[74:75], v[128:129]
	v_pk_fma_f32 v[2:3], v[110:111], v[12:13], v[126:127]
	v_pk_mul_f32 v[12:13], v[76:77], v[68:69] op_sel_hi:[1,0]
	v_cvt_pk_bf16_f32 v68, v2, v3
	v_cvt_pk_bf16_f32 v69, v4, v5
	v_pk_fma_f32 v[8:9], v[116:117], v[72:73], v[132:133]
	v_pk_fma_f32 v[6:7], v[114:115], v[12:13], v[130:131]
	v_pk_fma_f32 v[12:13], v[120:121], v[10:11], v[136:137]
	v_pk_fma_f32 v[10:11], v[118:119], v[70:71], v[134:135]
	v_pk_fma_f32 v[16:17], v[124:125], v[16:17], v[140:141]
	global_store_dwordx2 v[24:25], v[68:69], off offset:-1024
	v_cvt_pk_bf16_f32 v68, v6, v7
	v_cvt_pk_bf16_f32 v69, v8, v9
	v_pk_fma_f32 v[14:15], v[122:123], v[14:15], v[138:139]
	global_store_dwordx2 v[24:25], v[68:69], off offset:-512
	v_cvt_pk_bf16_f32 v68, v10, v11
	v_cvt_pk_bf16_f32 v69, v12, v13
	global_store_dwordx2 v[24:25], v[68:69], off
	v_cvt_pk_bf16_f32 v68, v14, v15
	v_cvt_pk_bf16_f32 v69, v16, v17
	global_store_dwordx2 v[24:25], v[68:69], off offset:512
	s_waitcnt vmcnt(4)
	s_cbranch_vccnz .LBB0_1234
	global_store_dwordx4 v[26:27], v[2:5], off offset:-2048 nt
	global_store_dwordx4 v[26:27], v[6:9], off offset:-1024 nt
	global_store_dwordx4 v[26:27], v[10:13], off nt
	global_store_dwordx4 v[26:27], v[14:17], off offset:1024 nt
	s_branch .LBB0_1234
